# even in-projection epilogue: dropped the seven repeated vmcnt(0) that could only wait for the previous store group
# speedup vs baseline: 1.0045x; 1.0045x over previous
; __device__ __forceinline__ void st16_wt(void* p, u32x4 v) { asm volatile("global_store_dwordx4 %0, %1, off sc1\n\ts_nop 1" :: "v"(p), "v"(v) : "memory"); }
; __device__ __forceinline__ unsigned cvt_pk_bf16(float lo, float hi) { unsigned r; asm volatile("v_cvt_pk_bf16_f32 %0, %1, %2" : "=v"(r) : "v"(lo), "v"(hi)); return r; }
;     __device__ __forceinline__ void operator()(const Acc& acc, const Unit& u, int wr, int wc, int fr, int fq, const LAS float* tab) const {
;     ...
;                 const int rl = ai * HALF + wr * 64 + m * 16 + fr; const size_t row = (size_t)u.pm * BM + rl; const float rs = rsv[ai][m];
;                 f32x4 v[2][2]; float ss = 0.f;
; #pragma unroll
;                 for (int bj = 0; bj < 2; ++bj)
; #pragma unroll
;                     for (int n = 0; n < 2; ++n) { v[bj][n] = acc[ai][bj][m][n] * rs; const f32x4 x = v[bj][n]; ss += (x[0] * x[0] + x[1] * x[1]) + (x[2] * x[2] + x[3] * x[3]); }
;                 if (mode == 3) { if (fq == 0) *(f32x4*)(WI + row * 4) = v[0][0]; continue; }
;                 float sc = 1.f;
;                 if (mode == 1 || mode == 2) { ss = sum_rows4(ss); sc = rsqrtf(ss * (1.0f / 64.0f) + EPS); if (mode == 1) sc *= C2; }
; #pragma unroll
;                 for (int bj = 0; bj < 2; ++bj) { const f32x4 a = v[bj][0] * gv[bj][0] * sc, b = v[bj][1] * gv[bj][1] * sc;
;                     u32x4 w; w.x = cvt_pk_bf16(a[0], a[1]); w.y = cvt_pk_bf16(a[2], a[3]); w.z = cvt_pk_bf16(b[0], b[1]); w.w = cvt_pk_bf16(b[2], b[3]);
;                     st16_wt(dst + row * pitch + 32 * bj + 8 * fq, w); }
.LBB0_582:
	v_mul_lo_u32 v134, s43, v130
	v_mul_lo_u32 v135, s42, v131
	v_mad_u64_u32 v[132:133], s[0:1], s42, v130, 0
	v_add3_u32 v133, v133, v135, v134
	v_pk_mul_f32 v[134:135], v[84:85], v[128:129]
	v_pk_mul_f32 v[136:137], v[82:83], v[126:127]
	v_pk_mul_f32 v[124:125], v[92:93], v[124:125]
	v_pk_mul_f32 v[122:123], v[90:91], v[122:123]
	v_pk_mul_f32 v[134:135], v[134:135], v[0:1] op_sel_hi:[1,0]
	v_pk_mul_f32 v[136:137], v[136:137], v[0:1] op_sel_hi:[1,0]
	v_pk_mul_f32 v[138:139], v[124:125], v[0:1] op_sel_hi:[1,0]
	v_pk_mul_f32 v[124:125], v[122:123], v[0:1] op_sel_hi:[1,0]
	v_cvt_pk_bf16_f32 v122, v136, v137
	v_cvt_pk_bf16_f32 v123, v134, v135
	v_pk_mul_f32 v[118:119], v[102:103], v[118:119]
	v_pk_mul_f32 v[116:117], v[112:113], v[116:117]
	v_pk_mul_f32 v[114:115], v[110:111], v[114:115]
	v_lshl_add_u64 v[132:133], v[132:133], 1, v[178:179]
	v_cvt_pk_bf16_f32 v124, v124, v125
	v_cvt_pk_bf16_f32 v125, v138, v139
	v_pk_mul_f32 v[120:121], v[104:105], v[120:121]
	global_store_dwordx4 v[132:133], v[122:125], off sc1
	s_nop 1
	v_pk_mul_f32 v[118:119], v[118:119], v[0:1] op_sel_hi:[1,0]
	v_pk_mul_f32 v[122:123], v[116:117], v[0:1] op_sel_hi:[1,0]
	v_pk_mul_f32 v[116:117], v[114:115], v[0:1] op_sel_hi:[1,0]
	v_pk_mul_f32 v[120:121], v[120:121], v[0:1] op_sel_hi:[1,0]
	v_cvt_pk_bf16_f32 v114, v118, v119
	v_lshl_add_u64 v[118:119], v[132:133], 0, 64
	v_cvt_pk_bf16_f32 v115, v120, v121
	v_cvt_pk_bf16_f32 v116, v116, v117
	v_cvt_pk_bf16_f32 v117, v122, v123
	s_mov_b64 s[48:49], 0
	global_store_dwordx4 v[118:119], v[114:117], off sc1
	s_nop 1

; __device__ __forceinline__ void st16_wt(void* p, u32x4 v) { asm volatile("global_store_dwordx4 %0, %1, off sc1\n\ts_nop 1" :: "v"(p), "v"(v) : "memory"); }
; __device__ __forceinline__ unsigned cvt_pk_bf16(float lo, float hi) { unsigned r; asm volatile("v_cvt_pk_bf16_f32 %0, %1, %2" : "=v"(r) : "v"(lo), "v"(hi)); return r; }
;     __device__ __forceinline__ void operator()(const Acc& acc, const Unit& u, int wr, int wc, int fr, int fq, const LAS float* tab) const {
;     ...
;                 const int rl = ai * HALF + wr * 64 + m * 16 + fr; const size_t row = (size_t)u.pm * BM + rl; const float rs = rsv[ai][m];
;                 f32x4 v[2][2]; float ss = 0.f;
; #pragma unroll
;                 for (int bj = 0; bj < 2; ++bj)
; #pragma unroll
;                     for (int n = 0; n < 2; ++n) { v[bj][n] = acc[ai][bj][m][n] * rs; const f32x4 x = v[bj][n]; ss += (x[0] * x[0] + x[1] * x[1]) + (x[2] * x[2] + x[3] * x[3]); }
;                 if (mode == 3) { if (fq == 0) *(f32x4*)(WI + row * 4) = v[0][0]; continue; }
;                 float sc = 1.f;
;                 if (mode == 1 || mode == 2) { ss = sum_rows4(ss); sc = rsqrtf(ss * (1.0f / 64.0f) + EPS); if (mode == 1) sc *= C2; }
; #pragma unroll
;                 for (int bj = 0; bj < 2; ++bj) { const f32x4 a = v[bj][0] * gv[bj][0] * sc, b = v[bj][1] * gv[bj][1] * sc;
;                     u32x4 w; w.x = cvt_pk_bf16(a[0], a[1]); w.y = cvt_pk_bf16(a[2], a[3]); w.z = cvt_pk_bf16(b[0], b[1]); w.w = cvt_pk_bf16(b[2], b[3]);
;                     st16_wt(dst + row * pitch + 32 * bj + 8 * fq, w); }
.LBB0_590:
	v_mul_lo_u32 v118, s43, v114
	v_mul_lo_u32 v119, s42, v115
	v_mad_u64_u32 v[116:117], s[0:1], s42, v114, 0
	v_add3_u32 v117, v117, v119, v118
	v_pk_mul_f32 v[118:119], v[84:85], v[108:109]
	v_pk_mul_f32 v[120:121], v[82:83], v[106:107]
	v_pk_mul_f32 v[100:101], v[92:93], v[100:101]
	v_pk_mul_f32 v[98:99], v[90:91], v[98:99]
	v_pk_mul_f32 v[118:119], v[118:119], v[0:1] op_sel_hi:[1,0]
	v_pk_mul_f32 v[120:121], v[120:121], v[0:1] op_sel_hi:[1,0]
	v_pk_mul_f32 v[122:123], v[100:101], v[0:1] op_sel_hi:[1,0]
	v_pk_mul_f32 v[100:101], v[98:99], v[0:1] op_sel_hi:[1,0]
	v_cvt_pk_bf16_f32 v98, v120, v121
	v_cvt_pk_bf16_f32 v99, v118, v119
	v_pk_mul_f32 v[94:95], v[102:103], v[94:95]
	v_pk_mul_f32 v[88:89], v[112:113], v[88:89]
	v_pk_mul_f32 v[86:87], v[110:111], v[86:87]
	v_lshl_add_u64 v[116:117], v[116:117], 1, v[178:179]
	v_cvt_pk_bf16_f32 v100, v100, v101
	v_cvt_pk_bf16_f32 v101, v122, v123
	v_pk_mul_f32 v[96:97], v[104:105], v[96:97]
	global_store_dwordx4 v[116:117], v[98:101], off sc1
	s_nop 1
	v_pk_mul_f32 v[94:95], v[94:95], v[0:1] op_sel_hi:[1,0]
	v_pk_mul_f32 v[98:99], v[88:89], v[0:1] op_sel_hi:[1,0]
	v_pk_mul_f32 v[88:89], v[86:87], v[0:1] op_sel_hi:[1,0]
	v_pk_mul_f32 v[96:97], v[96:97], v[0:1] op_sel_hi:[1,0]
	v_cvt_pk_bf16_f32 v86, v94, v95
	v_lshl_add_u64 v[94:95], v[116:117], 0, 64
	v_cvt_pk_bf16_f32 v87, v96, v97
	v_cvt_pk_bf16_f32 v88, v88, v89
	v_cvt_pk_bf16_f32 v89, v98, v99
	s_mov_b64 s[48:49], 0
	global_store_dwordx4 v[94:95], v[86:89], off sc1
	s_nop 1

; __device__ __forceinline__ void st16_wt(void* p, u32x4 v) { asm volatile("global_store_dwordx4 %0, %1, off sc1\n\ts_nop 1" :: "v"(p), "v"(v) : "memory"); }
; __device__ __forceinline__ unsigned cvt_pk_bf16(float lo, float hi) { unsigned r; asm volatile("v_cvt_pk_bf16_f32 %0, %1, %2" : "=v"(r) : "v"(lo), "v"(hi)); return r; }
;     __device__ __forceinline__ void operator()(const Acc& acc, const Unit& u, int wr, int wc, int fr, int fq, const LAS float* tab) const {
;     ...
;                 const int rl = ai * HALF + wr * 64 + m * 16 + fr; const size_t row = (size_t)u.pm * BM + rl; const float rs = rsv[ai][m];
;                 f32x4 v[2][2]; float ss = 0.f;
; #pragma unroll
;                 for (int bj = 0; bj < 2; ++bj)
; #pragma unroll
;                     for (int n = 0; n < 2; ++n) { v[bj][n] = acc[ai][bj][m][n] * rs; const f32x4 x = v[bj][n]; ss += (x[0] * x[0] + x[1] * x[1]) + (x[2] * x[2] + x[3] * x[3]); }
;                 if (mode == 3) { if (fq == 0) *(f32x4*)(WI + row * 4) = v[0][0]; continue; }
;                 float sc = 1.f;
;                 if (mode == 1 || mode == 2) { ss = sum_rows4(ss); sc = rsqrtf(ss * (1.0f / 64.0f) + EPS); if (mode == 1) sc *= C2; }
; #pragma unroll
;                 for (int bj = 0; bj < 2; ++bj) { const f32x4 a = v[bj][0] * gv[bj][0] * sc, b = v[bj][1] * gv[bj][1] * sc;
;                     u32x4 w; w.x = cvt_pk_bf16(a[0], a[1]); w.y = cvt_pk_bf16(a[2], a[3]); w.z = cvt_pk_bf16(b[0], b[1]); w.w = cvt_pk_bf16(b[2], b[3]);
;                     st16_wt(dst + row * pitch + 32 * bj + 8 * fq, w); }
.LBB0_598:
	v_mul_lo_u32 v94, s43, v86
	v_mul_lo_u32 v95, s42, v87
	v_mad_u64_u32 v[88:89], s[0:1], s42, v86, 0
	v_add3_u32 v89, v89, v95, v94
	v_pk_mul_f32 v[94:95], v[84:85], v[80:81]
	v_pk_mul_f32 v[96:97], v[82:83], v[78:79]
	v_pk_mul_f32 v[76:77], v[92:93], v[76:77]
	v_pk_mul_f32 v[74:75], v[90:91], v[74:75]
	v_pk_mul_f32 v[94:95], v[94:95], v[0:1] op_sel_hi:[1,0]
	v_pk_mul_f32 v[96:97], v[96:97], v[0:1] op_sel_hi:[1,0]
	v_pk_mul_f32 v[98:99], v[76:77], v[0:1] op_sel_hi:[1,0]
	v_pk_mul_f32 v[76:77], v[74:75], v[0:1] op_sel_hi:[1,0]
	v_cvt_pk_bf16_f32 v74, v96, v97
	v_cvt_pk_bf16_f32 v75, v94, v95
	v_pk_mul_f32 v[70:71], v[102:103], v[70:71]
	v_pk_mul_f32 v[68:69], v[112:113], v[68:69]
	v_pk_mul_f32 v[66:67], v[110:111], v[66:67]
	v_lshl_add_u64 v[88:89], v[88:89], 1, v[178:179]
	v_cvt_pk_bf16_f32 v76, v76, v77
	v_cvt_pk_bf16_f32 v77, v98, v99
	v_pk_mul_f32 v[72:73], v[104:105], v[72:73]
	global_store_dwordx4 v[88:89], v[74:77], off sc1
	s_nop 1
	v_pk_mul_f32 v[70:71], v[70:71], v[0:1] op_sel_hi:[1,0]
	v_pk_mul_f32 v[74:75], v[68:69], v[0:1] op_sel_hi:[1,0]
	v_pk_mul_f32 v[68:69], v[66:67], v[0:1] op_sel_hi:[1,0]
	v_pk_mul_f32 v[72:73], v[72:73], v[0:1] op_sel_hi:[1,0]
	v_cvt_pk_bf16_f32 v66, v70, v71
	v_lshl_add_u64 v[70:71], v[88:89], 0, 64
	v_cvt_pk_bf16_f32 v67, v72, v73
	v_cvt_pk_bf16_f32 v68, v68, v69
	v_cvt_pk_bf16_f32 v69, v74, v75
	s_mov_b64 s[48:49], 0
	global_store_dwordx4 v[70:71], v[66:69], off sc1
	s_nop 1

; __device__ __forceinline__ void st16_wt(void* p, u32x4 v) { asm volatile("global_store_dwordx4 %0, %1, off sc1\n\ts_nop 1" :: "v"(p), "v"(v) : "memory"); }
; __device__ __forceinline__ unsigned cvt_pk_bf16(float lo, float hi) { unsigned r; asm volatile("v_cvt_pk_bf16_f32 %0, %1, %2" : "=v"(r) : "v"(lo), "v"(hi)); return r; }
;     __device__ __forceinline__ void operator()(const Acc& acc, const Unit& u, int wr, int wc, int fr, int fq, const LAS float* tab) const {
;     ...
;                 const int rl = ai * HALF + wr * 64 + m * 16 + fr; const size_t row = (size_t)u.pm * BM + rl; const float rs = rsv[ai][m];
;                 f32x4 v[2][2]; float ss = 0.f;
; #pragma unroll
;                 for (int bj = 0; bj < 2; ++bj)
; #pragma unroll
;                     for (int n = 0; n < 2; ++n) { v[bj][n] = acc[ai][bj][m][n] * rs; const f32x4 x = v[bj][n]; ss += (x[0] * x[0] + x[1] * x[1]) + (x[2] * x[2] + x[3] * x[3]); }
;                 if (mode == 3) { if (fq == 0) *(f32x4*)(WI + row * 4) = v[0][0]; continue; }
;                 float sc = 1.f;
;                 if (mode == 1 || mode == 2) { ss = sum_rows4(ss); sc = rsqrtf(ss * (1.0f / 64.0f) + EPS); if (mode == 1) sc *= C2; }
; #pragma unroll
;                 for (int bj = 0; bj < 2; ++bj) { const f32x4 a = v[bj][0] * gv[bj][0] * sc, b = v[bj][1] * gv[bj][1] * sc;
;                     u32x4 w; w.x = cvt_pk_bf16(a[0], a[1]); w.y = cvt_pk_bf16(a[2], a[3]); w.z = cvt_pk_bf16(b[0], b[1]); w.w = cvt_pk_bf16(b[2], b[3]);
;                     st16_wt(dst + row * pitch + 32 * bj + 8 * fq, w); }
.LBB0_606:
	v_mul_lo_u32 v70, s43, v66
	v_mul_lo_u32 v71, s42, v67
	v_mad_u64_u32 v[68:69], s[0:1], s42, v66, 0
	v_add3_u32 v69, v69, v71, v70
	v_pk_mul_f32 v[70:71], v[84:85], v[64:65]
	v_pk_mul_f32 v[72:73], v[82:83], v[62:63]
	v_pk_mul_f32 v[60:61], v[92:93], v[60:61]
	v_pk_mul_f32 v[58:59], v[90:91], v[58:59]
	v_pk_mul_f32 v[70:71], v[70:71], v[0:1] op_sel_hi:[1,0]
	v_pk_mul_f32 v[72:73], v[72:73], v[0:1] op_sel_hi:[1,0]
	v_pk_mul_f32 v[74:75], v[60:61], v[0:1] op_sel_hi:[1,0]
	v_pk_mul_f32 v[60:61], v[58:59], v[0:1] op_sel_hi:[1,0]
	v_cvt_pk_bf16_f32 v58, v72, v73
	v_cvt_pk_bf16_f32 v59, v70, v71
	v_pk_mul_f32 v[54:55], v[102:103], v[54:55]
	v_pk_mul_f32 v[52:53], v[112:113], v[52:53]
	v_pk_mul_f32 v[50:51], v[110:111], v[50:51]
	v_lshl_add_u64 v[68:69], v[68:69], 1, v[178:179]
	v_cvt_pk_bf16_f32 v60, v60, v61
	v_cvt_pk_bf16_f32 v61, v74, v75
	v_pk_mul_f32 v[56:57], v[104:105], v[56:57]
	global_store_dwordx4 v[68:69], v[58:61], off sc1
	s_nop 1
	v_pk_mul_f32 v[54:55], v[54:55], v[0:1] op_sel_hi:[1,0]
	v_pk_mul_f32 v[58:59], v[52:53], v[0:1] op_sel_hi:[1,0]
	v_pk_mul_f32 v[52:53], v[50:51], v[0:1] op_sel_hi:[1,0]
	v_pk_mul_f32 v[56:57], v[56:57], v[0:1] op_sel_hi:[1,0]
	v_cvt_pk_bf16_f32 v50, v54, v55
	v_lshl_add_u64 v[54:55], v[68:69], 0, 64
	v_cvt_pk_bf16_f32 v51, v56, v57
	v_cvt_pk_bf16_f32 v52, v52, v53
	v_cvt_pk_bf16_f32 v53, v58, v59
	s_mov_b64 s[48:49], 0
	global_store_dwordx4 v[54:55], v[50:53], off sc1
	s_nop 1

; __device__ __forceinline__ void st16_wt(void* p, u32x4 v) { asm volatile("global_store_dwordx4 %0, %1, off sc1\n\ts_nop 1" :: "v"(p), "v"(v) : "memory"); }
; __device__ __forceinline__ unsigned cvt_pk_bf16(float lo, float hi) { unsigned r; asm volatile("v_cvt_pk_bf16_f32 %0, %1, %2" : "=v"(r) : "v"(lo), "v"(hi)); return r; }
;     __device__ __forceinline__ void operator()(const Acc& acc, const Unit& u, int wr, int wc, int fr, int fq, const LAS float* tab) const {
;     ...
;                 const int rl = ai * HALF + wr * 64 + m * 16 + fr; const size_t row = (size_t)u.pm * BM + rl; const float rs = rsv[ai][m];
;                 f32x4 v[2][2]; float ss = 0.f;
; #pragma unroll
;                 for (int bj = 0; bj < 2; ++bj)
; #pragma unroll
;                     for (int n = 0; n < 2; ++n) { v[bj][n] = acc[ai][bj][m][n] * rs; const f32x4 x = v[bj][n]; ss += (x[0] * x[0] + x[1] * x[1]) + (x[2] * x[2] + x[3] * x[3]); }
;                 if (mode == 3) { if (fq == 0) *(f32x4*)(WI + row * 4) = v[0][0]; continue; }
;                 float sc = 1.f;
;                 if (mode == 1 || mode == 2) { ss = sum_rows4(ss); sc = rsqrtf(ss * (1.0f / 64.0f) + EPS); if (mode == 1) sc *= C2; }
; #pragma unroll
;                 for (int bj = 0; bj < 2; ++bj) { const f32x4 a = v[bj][0] * gv[bj][0] * sc, b = v[bj][1] * gv[bj][1] * sc;
;                     u32x4 w; w.x = cvt_pk_bf16(a[0], a[1]); w.y = cvt_pk_bf16(a[2], a[3]); w.z = cvt_pk_bf16(b[0], b[1]); w.w = cvt_pk_bf16(b[2], b[3]);
;                     st16_wt(dst + row * pitch + 32 * bj + 8 * fq, w); }
.LBB0_614:
	v_mul_lo_u32 v54, s43, v50
	v_mul_lo_u32 v55, s42, v51
	v_mad_u64_u32 v[52:53], s[0:1], s42, v50, 0
	v_add3_u32 v53, v53, v55, v54
	v_pk_mul_f32 v[54:55], v[84:85], v[48:49]
	v_pk_mul_f32 v[56:57], v[82:83], v[46:47]
	v_pk_mul_f32 v[44:45], v[92:93], v[44:45]
	v_pk_mul_f32 v[42:43], v[90:91], v[42:43]
	v_pk_mul_f32 v[54:55], v[54:55], v[0:1] op_sel_hi:[1,0]
	v_pk_mul_f32 v[56:57], v[56:57], v[0:1] op_sel_hi:[1,0]
	v_pk_mul_f32 v[58:59], v[44:45], v[0:1] op_sel_hi:[1,0]
	v_pk_mul_f32 v[44:45], v[42:43], v[0:1] op_sel_hi:[1,0]
	v_cvt_pk_bf16_f32 v42, v56, v57
	v_cvt_pk_bf16_f32 v43, v54, v55
	v_pk_mul_f32 v[38:39], v[102:103], v[38:39]
	v_pk_mul_f32 v[36:37], v[112:113], v[36:37]
	v_pk_mul_f32 v[34:35], v[110:111], v[34:35]
	v_lshl_add_u64 v[52:53], v[52:53], 1, v[178:179]
	v_cvt_pk_bf16_f32 v44, v44, v45
	v_cvt_pk_bf16_f32 v45, v58, v59
	v_pk_mul_f32 v[40:41], v[104:105], v[40:41]
	global_store_dwordx4 v[52:53], v[42:45], off sc1
	s_nop 1
	v_pk_mul_f32 v[38:39], v[38:39], v[0:1] op_sel_hi:[1,0]
	v_pk_mul_f32 v[42:43], v[36:37], v[0:1] op_sel_hi:[1,0]
	v_pk_mul_f32 v[36:37], v[34:35], v[0:1] op_sel_hi:[1,0]
	v_pk_mul_f32 v[40:41], v[40:41], v[0:1] op_sel_hi:[1,0]
	v_cvt_pk_bf16_f32 v34, v38, v39
	v_lshl_add_u64 v[38:39], v[52:53], 0, 64
	v_cvt_pk_bf16_f32 v35, v40, v41
	v_cvt_pk_bf16_f32 v36, v36, v37
	v_cvt_pk_bf16_f32 v37, v42, v43
	s_mov_b64 s[48:49], 0
	global_store_dwordx4 v[38:39], v[34:37], off sc1
	s_nop 1

; __device__ __forceinline__ void st16_wt(void* p, u32x4 v) { asm volatile("global_store_dwordx4 %0, %1, off sc1\n\ts_nop 1" :: "v"(p), "v"(v) : "memory"); }
; __device__ __forceinline__ unsigned cvt_pk_bf16(float lo, float hi) { unsigned r; asm volatile("v_cvt_pk_bf16_f32 %0, %1, %2" : "=v"(r) : "v"(lo), "v"(hi)); return r; }
;     __device__ __forceinline__ void operator()(const Acc& acc, const Unit& u, int wr, int wc, int fr, int fq, const LAS float* tab) const {
;     ...
;                 const int rl = ai * HALF + wr * 64 + m * 16 + fr; const size_t row = (size_t)u.pm * BM + rl; const float rs = rsv[ai][m];
;                 f32x4 v[2][2]; float ss = 0.f;
; #pragma unroll
;                 for (int bj = 0; bj < 2; ++bj)
; #pragma unroll
;                     for (int n = 0; n < 2; ++n) { v[bj][n] = acc[ai][bj][m][n] * rs; const f32x4 x = v[bj][n]; ss += (x[0] * x[0] + x[1] * x[1]) + (x[2] * x[2] + x[3] * x[3]); }
;                 if (mode == 3) { if (fq == 0) *(f32x4*)(WI + row * 4) = v[0][0]; continue; }
;                 float sc = 1.f;
;                 if (mode == 1 || mode == 2) { ss = sum_rows4(ss); sc = rsqrtf(ss * (1.0f / 64.0f) + EPS); if (mode == 1) sc *= C2; }
; #pragma unroll
;                 for (int bj = 0; bj < 2; ++bj) { const f32x4 a = v[bj][0] * gv[bj][0] * sc, b = v[bj][1] * gv[bj][1] * sc;
;                     u32x4 w; w.x = cvt_pk_bf16(a[0], a[1]); w.y = cvt_pk_bf16(a[2], a[3]); w.z = cvt_pk_bf16(b[0], b[1]); w.w = cvt_pk_bf16(b[2], b[3]);
;                     st16_wt(dst + row * pitch + 32 * bj + 8 * fq, w); }
.LBB0_622:
	v_mul_lo_u32 v38, s43, v34
	v_mul_lo_u32 v39, s42, v35
	v_mad_u64_u32 v[36:37], s[0:1], s42, v34, 0
	v_add3_u32 v37, v37, v39, v38
	v_pk_mul_f32 v[38:39], v[84:85], v[32:33]
	v_pk_mul_f32 v[40:41], v[82:83], v[30:31]
	v_pk_mul_f32 v[28:29], v[92:93], v[28:29]
	v_pk_mul_f32 v[26:27], v[90:91], v[26:27]
	v_pk_mul_f32 v[38:39], v[38:39], v[0:1] op_sel_hi:[1,0]
	v_pk_mul_f32 v[40:41], v[40:41], v[0:1] op_sel_hi:[1,0]
	v_pk_mul_f32 v[42:43], v[28:29], v[0:1] op_sel_hi:[1,0]
	v_pk_mul_f32 v[28:29], v[26:27], v[0:1] op_sel_hi:[1,0]
	v_cvt_pk_bf16_f32 v26, v40, v41
	v_cvt_pk_bf16_f32 v27, v38, v39
	v_pk_mul_f32 v[22:23], v[102:103], v[22:23]
	v_pk_mul_f32 v[20:21], v[112:113], v[20:21]
	v_pk_mul_f32 v[18:19], v[110:111], v[18:19]
	v_lshl_add_u64 v[36:37], v[36:37], 1, v[178:179]
	v_cvt_pk_bf16_f32 v28, v28, v29
	v_cvt_pk_bf16_f32 v29, v42, v43
	v_pk_mul_f32 v[24:25], v[104:105], v[24:25]
	global_store_dwordx4 v[36:37], v[26:29], off sc1
	s_nop 1
	v_pk_mul_f32 v[22:23], v[22:23], v[0:1] op_sel_hi:[1,0]
	v_pk_mul_f32 v[26:27], v[20:21], v[0:1] op_sel_hi:[1,0]
	v_pk_mul_f32 v[20:21], v[18:19], v[0:1] op_sel_hi:[1,0]
	v_pk_mul_f32 v[24:25], v[24:25], v[0:1] op_sel_hi:[1,0]
	v_cvt_pk_bf16_f32 v18, v22, v23
	v_lshl_add_u64 v[22:23], v[36:37], 0, 64
	v_cvt_pk_bf16_f32 v19, v24, v25
	v_cvt_pk_bf16_f32 v20, v20, v21
	v_cvt_pk_bf16_f32 v21, v26, v27
	s_mov_b64 s[48:49], 0
	global_store_dwordx4 v[22:23], v[18:21], off sc1
	s_nop 1

; __device__ __forceinline__ void st16_wt(void* p, u32x4 v) { asm volatile("global_store_dwordx4 %0, %1, off sc1\n\ts_nop 1" :: "v"(p), "v"(v) : "memory"); }
; __device__ __forceinline__ unsigned cvt_pk_bf16(float lo, float hi) { unsigned r; asm volatile("v_cvt_pk_bf16_f32 %0, %1, %2" : "=v"(r) : "v"(lo), "v"(hi)); return r; }
;     __device__ __forceinline__ void operator()(const Acc& acc, const Unit& u, int wr, int wc, int fr, int fq, const LAS float* tab) const {
;     ...
;                 const int rl = ai * HALF + wr * 64 + m * 16 + fr; const size_t row = (size_t)u.pm * BM + rl; const float rs = rsv[ai][m];
;                 f32x4 v[2][2]; float ss = 0.f;
; #pragma unroll
;                 for (int bj = 0; bj < 2; ++bj)
; #pragma unroll
;                     for (int n = 0; n < 2; ++n) { v[bj][n] = acc[ai][bj][m][n] * rs; const f32x4 x = v[bj][n]; ss += (x[0] * x[0] + x[1] * x[1]) + (x[2] * x[2] + x[3] * x[3]); }
;                 if (mode == 3) { if (fq == 0) *(f32x4*)(WI + row * 4) = v[0][0]; continue; }
;                 float sc = 1.f;
;                 if (mode == 1 || mode == 2) { ss = sum_rows4(ss); sc = rsqrtf(ss * (1.0f / 64.0f) + EPS); if (mode == 1) sc *= C2; }
; #pragma unroll
;                 for (int bj = 0; bj < 2; ++bj) { const f32x4 a = v[bj][0] * gv[bj][0] * sc, b = v[bj][1] * gv[bj][1] * sc;
;                     u32x4 w; w.x = cvt_pk_bf16(a[0], a[1]); w.y = cvt_pk_bf16(a[2], a[3]); w.z = cvt_pk_bf16(b[0], b[1]); w.w = cvt_pk_bf16(b[2], b[3]);
;                     st16_wt(dst + row * pitch + 32 * bj + 8 * fq, w); }
.LBB0_630:
	v_mul_lo_u32 v22, s43, v18
	v_mul_lo_u32 v23, s42, v19
	v_mad_u64_u32 v[20:21], s[0:1], s42, v18, 0
	v_add3_u32 v21, v21, v23, v22
	v_pk_mul_f32 v[22:23], v[84:85], v[16:17]
	v_pk_mul_f32 v[24:25], v[82:83], v[14:15]
	v_pk_mul_f32 v[12:13], v[92:93], v[12:13]
	v_pk_mul_f32 v[10:11], v[90:91], v[10:11]
	v_pk_mul_f32 v[22:23], v[22:23], v[0:1] op_sel_hi:[1,0]
	v_pk_mul_f32 v[24:25], v[24:25], v[0:1] op_sel_hi:[1,0]
	v_pk_mul_f32 v[26:27], v[12:13], v[0:1] op_sel_hi:[1,0]
	v_pk_mul_f32 v[12:13], v[10:11], v[0:1] op_sel_hi:[1,0]
	v_cvt_pk_bf16_f32 v10, v24, v25
	v_cvt_pk_bf16_f32 v11, v22, v23
	v_pk_mul_f32 v[6:7], v[102:103], v[6:7]
	v_pk_mul_f32 v[4:5], v[112:113], v[4:5]
	v_pk_mul_f32 v[2:3], v[110:111], v[2:3]
	v_lshl_add_u64 v[20:21], v[20:21], 1, v[178:179]
	v_cvt_pk_bf16_f32 v12, v12, v13
	v_cvt_pk_bf16_f32 v13, v26, v27
	v_pk_mul_f32 v[8:9], v[104:105], v[8:9]
	global_store_dwordx4 v[20:21], v[10:13], off sc1
	s_nop 1
	v_pk_mul_f32 v[6:7], v[6:7], v[0:1] op_sel_hi:[1,0]
	v_pk_mul_f32 v[10:11], v[4:5], v[0:1] op_sel_hi:[1,0]
	v_pk_mul_f32 v[4:5], v[2:3], v[0:1] op_sel_hi:[1,0]
	v_pk_mul_f32 v[8:9], v[8:9], v[0:1] op_sel_hi:[1,0]
	v_cvt_pk_bf16_f32 v2, v6, v7
	v_lshl_add_u64 v[6:7], v[20:21], 0, 64
	v_cvt_pk_bf16_f32 v3, v8, v9
	v_cvt_pk_bf16_f32 v4, v4, v5
	v_cvt_pk_bf16_f32 v5, v10, v11
	s_mov_b64 s[12:13], 0
	global_store_dwordx4 v[6:7], v[2:5], off sc1
	s_nop 1
